# v3 + de-serialised expert-list lookups at the head of each MoE gate/up unit and the context side-tile residual epilogue (loads issued together, one wait)
# speedup vs baseline: 1.0916x; 1.0008x over previous
.LBB0_1382:
	s_nop 1
	ds_read_b128 v[100:103], v96
	ds_read_b128 v[104:107], v97 offset:17408
	s_min_u32 s8, s1, 2
	s_lshl_b32 s12, s8, 8
	s_or_b32 s1, s1, 1
	s_min_u32 s1, s1, 2
	s_waitcnt lgkmcnt(0)
	v_mfma_f32_16x16x32_bf16 v[68:71], v[100:103], v[104:107], v[68:71]
	ds_read_b128 v[104:107], v97 offset:21760
	s_and_b64 vcc, exec, s[4:5]
	s_mov_b64 s[4:5], 0
	s_waitcnt lgkmcnt(0)
	v_mfma_f32_16x16x32_bf16 v[64:67], v[100:103], v[104:107], v[64:67]
	ds_read_b128 v[100:103], v96 offset:64
	ds_read_b128 v[104:107], v97 offset:17472
	s_waitcnt lgkmcnt(0)
	v_mfma_f32_16x16x32_bf16 v[68:71], v[100:103], v[104:107], v[68:71]
	ds_read_b128 v[104:107], v97 offset:21824
	s_waitcnt lgkmcnt(0)
	v_mfma_f32_16x16x32_bf16 v[64:67], v[100:103], v[104:107], v[64:67]
	ds_read_b128 v[100:103], v96 offset:128
	ds_read_b128 v[104:107], v97 offset:17536
	s_waitcnt lgkmcnt(0)
	v_mfma_f32_16x16x32_bf16 v[68:71], v[100:103], v[104:107], v[68:71]
	ds_read_b128 v[104:107], v97 offset:21888
	s_waitcnt lgkmcnt(0)
	v_mfma_f32_16x16x32_bf16 v[64:67], v[100:103], v[104:107], v[64:67]
	ds_read_b128 v[100:103], v96 offset:192
	ds_read_b128 v[104:107], v97 offset:17600
	s_waitcnt lgkmcnt(0)
	v_mfma_f32_16x16x32_bf16 v[68:71], v[100:103], v[104:107], v[68:71]
	ds_read_b128 v[104:107], v97 offset:21952
	s_waitcnt vmcnt(15)
	ds_write_b128 v98, v[0:3] offset:34816
	s_waitcnt vmcnt(14)
	ds_write_b128 v98, v[4:7] offset:52224
	s_waitcnt vmcnt(13)
	ds_write_b128 v99, v[8:11] offset:34816
	s_waitcnt vmcnt(12)
	ds_write_b128 v99, v[12:15] offset:52224
	v_lshl_add_u64 v[8:9], v[82:83], 0, s[12:13]
	v_lshl_add_u64 v[12:13], v[84:85], 0, s[12:13]
	v_lshl_add_u64 v[0:1], v[8:9], 0, v[78:79]
	v_lshl_add_u64 v[4:5], v[12:13], 0, v[78:79]
	v_lshl_add_u64 v[8:9], v[8:9], 0, v[80:81]
	v_lshl_add_u64 v[12:13], v[12:13], 0, v[80:81]
	global_load_dwordx4 v[0:3], v[0:1], off offset:1280
	s_waitcnt lgkmcnt(4)
	v_mfma_f32_16x16x32_bf16 v[64:67], v[100:103], v[104:107], v[64:67]
	global_load_dwordx4 v[4:7], v[4:5], off offset:1280
	s_lshl_b32 s12, s1, 8
	global_load_dwordx4 v[8:11], v[8:9], off offset:1280
	s_mov_b32 s1, 4
	global_load_dwordx4 v[12:15], v[12:13], off offset:1280
	s_waitcnt lgkmcnt(0)
	s_barrier
	ds_read_b128 v[100:103], v96 offset:34816
	ds_read_b128 v[104:107], v97 offset:52224
	s_waitcnt lgkmcnt(0)
	v_mfma_f32_16x16x32_bf16 v[68:71], v[100:103], v[104:107], v[68:71]
	ds_read_b128 v[104:107], v97 offset:56576
	s_waitcnt lgkmcnt(0)
	v_mfma_f32_16x16x32_bf16 v[64:67], v[100:103], v[104:107], v[64:67]
	ds_read_b128 v[100:103], v96 offset:34880
	ds_read_b128 v[104:107], v97 offset:52288
	s_waitcnt lgkmcnt(0)
	v_mfma_f32_16x16x32_bf16 v[68:71], v[100:103], v[104:107], v[68:71]
	ds_read_b128 v[104:107], v97 offset:56640
	s_waitcnt lgkmcnt(0)
	v_mfma_f32_16x16x32_bf16 v[64:67], v[100:103], v[104:107], v[64:67]
	ds_read_b128 v[100:103], v96 offset:34944
	ds_read_b128 v[104:107], v97 offset:52352
	s_waitcnt lgkmcnt(0)
	v_mfma_f32_16x16x32_bf16 v[68:71], v[100:103], v[104:107], v[68:71]
	ds_read_b128 v[104:107], v97 offset:56704
	s_waitcnt lgkmcnt(0)
	v_mfma_f32_16x16x32_bf16 v[100:103], v[100:103], v[104:107], v[64:67]
	ds_read_b128 v[104:107], v96 offset:35008
	s_nop 1
	ds_read_b128 v[64:67], v97 offset:52416
	s_waitcnt lgkmcnt(0)
	v_mfma_f32_16x16x32_bf16 v[64:67], v[104:107], v[64:67], v[68:71]
	s_nop 2
	ds_read_b128 v[68:71], v97 offset:56768
	s_waitcnt vmcnt(15)
	ds_write_b128 v98, v[48:51]
	s_waitcnt vmcnt(14)
	ds_write_b128 v98, v[52:55] offset:17408
	s_waitcnt vmcnt(13)
	ds_write_b128 v99, v[56:59]
	s_waitcnt vmcnt(12)
	ds_write_b128 v99, v[60:63] offset:17408
	v_lshl_add_u64 v[56:57], v[82:83], 0, s[12:13]
	v_lshl_add_u64 v[60:61], v[84:85], 0, s[12:13]
	v_lshl_add_u64 v[48:49], v[56:57], 0, v[78:79]
	v_lshl_add_u64 v[52:53], v[60:61], 0, v[78:79]
	v_lshl_add_u64 v[56:57], v[56:57], 0, v[80:81]
	v_lshl_add_u64 v[60:61], v[60:61], 0, v[80:81]
	global_load_dwordx4 v[48:51], v[48:49], off offset:1280
	s_waitcnt lgkmcnt(4)
	v_mfma_f32_16x16x32_bf16 v[68:71], v[104:107], v[68:71], v[100:103]
	global_load_dwordx4 v[52:55], v[52:53], off offset:1280
	s_nop 0
	global_load_dwordx4 v[56:59], v[56:57], off offset:1280
	s_nop 0
	global_load_dwordx4 v[60:63], v[60:61], off offset:1280
	s_waitcnt lgkmcnt(0)
	s_barrier
	ds_read_b128 v[100:103], v96
	ds_read_b128 v[104:107], v97 offset:17408
	s_waitcnt lgkmcnt(0)
	v_mfma_f32_16x16x32_bf16 v[64:67], v[100:103], v[104:107], v[64:67]
	ds_read_b128 v[104:107], v97 offset:21760
	s_waitcnt lgkmcnt(0)
	v_mfma_f32_16x16x32_bf16 v[68:71], v[100:103], v[104:107], v[68:71]
	ds_read_b128 v[100:103], v96 offset:64
	ds_read_b128 v[104:107], v97 offset:17472
	s_waitcnt lgkmcnt(0)
	v_mfma_f32_16x16x32_bf16 v[64:67], v[100:103], v[104:107], v[64:67]
	ds_read_b128 v[104:107], v97 offset:21824
	s_waitcnt lgkmcnt(0)
	v_mfma_f32_16x16x32_bf16 v[68:71], v[100:103], v[104:107], v[68:71]
	ds_read_b128 v[100:103], v96 offset:128
	ds_read_b128 v[104:107], v97 offset:17536
	s_waitcnt lgkmcnt(0)
	v_mfma_f32_16x16x32_bf16 v[64:67], v[100:103], v[104:107], v[64:67]
	ds_read_b128 v[104:107], v97 offset:21888
	s_waitcnt lgkmcnt(0)
	v_mfma_f32_16x16x32_bf16 v[68:71], v[100:103], v[104:107], v[68:71]
	ds_read_b128 v[100:103], v96 offset:192
	ds_read_b128 v[104:107], v97 offset:17600
	s_waitcnt lgkmcnt(0)
	v_mfma_f32_16x16x32_bf16 v[64:67], v[100:103], v[104:107], v[64:67]
	ds_read_b128 v[104:107], v97 offset:21952
	s_waitcnt vmcnt(15)
	ds_write_b128 v98, v[16:19] offset:34816
	s_waitcnt vmcnt(14)
	ds_write_b128 v98, v[20:23] offset:52224
	s_waitcnt vmcnt(13)
	ds_write_b128 v99, v[28:31] offset:34816
	s_waitcnt vmcnt(12)
	ds_write_b128 v99, v[24:27] offset:52224
	global_load_dwordx4 v[16:19], v[86:87], off offset:1792
	global_load_dwordx4 v[20:23], v[88:89], off offset:1792
	global_load_dwordx4 v[28:31], v[90:91], off offset:1792
	global_load_dwordx4 v[24:27], v[92:93], off offset:1792
	s_waitcnt lgkmcnt(0)
	s_barrier
	s_waitcnt lgkmcnt(4)
	v_mfma_f32_16x16x32_bf16 v[68:71], v[100:103], v[104:107], v[68:71]
	ds_read_b128 v[100:103], v96 offset:34816
	ds_read_b128 v[104:107], v97 offset:52224
	s_waitcnt lgkmcnt(0)
	v_mfma_f32_16x16x32_bf16 v[64:67], v[100:103], v[104:107], v[64:67]
	ds_read_b128 v[104:107], v97 offset:56576
	s_waitcnt lgkmcnt(0)
	v_mfma_f32_16x16x32_bf16 v[68:71], v[100:103], v[104:107], v[68:71]
	ds_read_b128 v[100:103], v96 offset:34880
	ds_read_b128 v[104:107], v97 offset:52288
	s_waitcnt lgkmcnt(0)
	v_mfma_f32_16x16x32_bf16 v[64:67], v[100:103], v[104:107], v[64:67]
	ds_read_b128 v[104:107], v97 offset:56640
	s_waitcnt lgkmcnt(0)
	v_mfma_f32_16x16x32_bf16 v[68:71], v[100:103], v[104:107], v[68:71]
	ds_read_b128 v[100:103], v96 offset:34944
	ds_read_b128 v[104:107], v97 offset:52352
	s_waitcnt lgkmcnt(0)
	v_mfma_f32_16x16x32_bf16 v[64:67], v[100:103], v[104:107], v[64:67]
	ds_read_b128 v[104:107], v97 offset:56704
	s_waitcnt lgkmcnt(0)
	v_mfma_f32_16x16x32_bf16 v[100:103], v[100:103], v[104:107], v[68:71]
	ds_read_b128 v[104:107], v96 offset:35008
	s_nop 1
	ds_read_b128 v[68:71], v97 offset:52416
	s_waitcnt lgkmcnt(0)
	v_mfma_f32_16x16x32_bf16 v[68:71], v[104:107], v[68:71], v[64:67]
	s_nop 2
	ds_read_b128 v[64:67], v97 offset:56768
	s_waitcnt vmcnt(15)
	ds_write_b128 v98, v[36:39]
	s_waitcnt vmcnt(14)
	ds_write_b128 v98, v[32:35] offset:17408
	s_waitcnt vmcnt(13)
	ds_write_b128 v99, v[40:43]
	s_waitcnt vmcnt(12)
	ds_write_b128 v99, v[44:47] offset:17408
	global_load_dwordx4 v[36:39], v[86:87], off offset:1792
	global_load_dwordx4 v[32:35], v[88:89], off offset:1792
	global_load_dwordx4 v[40:43], v[90:91], off offset:1792
	global_load_dwordx4 v[44:47], v[92:93], off offset:1792
	s_waitcnt lgkmcnt(4)
	v_mfma_f32_16x16x32_bf16 v[64:67], v[104:107], v[64:67], v[100:103]
	s_waitcnt lgkmcnt(0)
	s_barrier
	s_cbranch_vccnz .LBB0_1382
	v_readlane_b32 s1, v253, 41
	s_add_i32 s7, s7, s1
	v_or_b32_e32 v0, s7, v94
	v_lshlrev_b32_e32 v0, 2, v0
	global_load_dword v6, v0, s[2:3]
	global_load_dword v7, v0, s[2:3] offset:64
	v_add_u32_e32 v0, s0, v95
	s_lshl_b32 s12, s7, 2
	v_ashrrev_i32_e32 v1, 31, v0
	v_lshl_add_u64 v[2:3], v[72:73], 0, s[12:13]
	v_lshlrev_b64 v[4:5], 12, v[0:1]
	v_lshl_add_u64 v[4:5], v[2:3], 0, v[4:5]
	v_add_co_u32_e32 v108, vcc, 0x1000, v4
	s_nop 0
	v_addc_co_u32_e32 v109, vcc, 0, v5, vcc
	v_add_co_u32_e32 v110, vcc, 0x3000, v4
	s_nop 0
	v_addc_co_u32_e32 v111, vcc, 0, v5, vcc
	global_load_dword v112, v[108:109], off offset:-4096
	global_load_dword v113, v[108:109], off offset:-4032
	global_load_dword v114, v[108:109], off
	global_load_dword v115, v[108:109], off offset:64
	global_load_dword v116, v[110:111], off offset:-4096
	global_load_dword v117, v[110:111], off offset:-4032
	global_load_dword v118, v[110:111], off
	global_load_dword v119, v[110:111], off offset:64
	v_readlane_b32 s0, v252, 5
	s_add_i32 s6, s6, s0
	s_waitcnt vmcnt(0)
	v_fmac_f32_e32 v112, v68, v6
	v_fmac_f32_e32 v113, v64, v7
	v_fmac_f32_e32 v114, v69, v6
	v_fmac_f32_e32 v115, v65, v7
	v_fmac_f32_e32 v116, v70, v6
	v_fmac_f32_e32 v117, v66, v7
	v_fmac_f32_e32 v118, v71, v6
	v_fmac_f32_e32 v119, v67, v7
	global_store_dword v[108:109], v112, off offset:-4096
	global_store_dword v[108:109], v113, off offset:-4032
	global_store_dword v[108:109], v114, off
	global_store_dword v[108:109], v115, off offset:64
	global_store_dword v[110:111], v116, off offset:-4096
	global_store_dword v[110:111], v117, off offset:-4032
	global_store_dword v[110:111], v118, off
	global_store_dword v[110:111], v119, off offset:64
	s_cmpk_lt_i32 s6, 0x100
	s_cbranch_scc1 .LBB0_1381

.LBB0_1617:
	s_andn2_b64 vcc, exec, s[4:5]
	s_cbranch_vccnz .LBB0_1657
	s_add_u32 s29, s20, 0x6a648200
	v_readlane_b32 s0, v252, 21
	s_addc_u32 s33, s21, 0
	s_lshl_b32 s34, s0, 10
	v_lshl_add_u32 v9, v4, 4, s34
	v_ashrrev_i32_e32 v0, 31, v9
	v_lshrrev_b32_e32 v0, 22, v0
	v_add_u32_e32 v0, v9, v0
	v_ashrrev_i32_e32 v3, 10, v0
	v_mul_i32_i24_e32 v0, 0x400, v3
	s_ashr_i32 s17, s16, 31
	v_sub_u32_e32 v0, v9, v0
	s_lshr_b32 s0, s17, 29
	v_lshrrev_b32_e32 v1, 4, v0
	s_add_i32 s0, s16, s0
	v_bitop3_b32 v5, v1, v0, 32 bitop3:0x6c
	s_ashr_i32 s0, s0, 3
	v_ashrrev_i32_e32 v1, 31, v5
	s_lshl_b32 s1, s0, 2
	v_lshrrev_b32_e32 v1, 26, v1
	s_add_i32 s1, s1, 0
	v_add_u32_e32 v1, v5, v1
	s_add_i32 s2, s1, 0x20100
	v_ashrrev_i32_e32 v2, 6, v1
	v_mov_b32_e32 v1, s2
	v_lshlrev_b32_e32 v0, 3, v3
	ds_read_b32 v1, v1
	v_and_b32_e32 v0, -16, v0
	s_add_i32 s1, s1, 0x201a0
	v_add_u32_e32 v152, v2, v0
	v_mov_b32_e32 v0, s1
	ds_read_b32 v8, v0
	s_waitcnt lgkmcnt(1)
	v_sub_u32_e32 v0, s49, v1
	v_lshlrev_b32_e32 v10, 8, v0
	s_mul_hi_i32 s1, s0, 0x11000
	s_mul_i32 s0, s0, 0x11000
	s_add_u32 s0, s29, s0
	v_add_u32_e32 v0, v10, v152
	s_addc_u32 s1, s33, s1
	s_waitcnt lgkmcnt(0)
	v_cmp_lt_i32_e32 vcc, v0, v8
	v_mov_b32_e32 v7, 0
	v_mov_b32_e32 v6, 0
	s_and_saveexec_b64 s[2:3], vcc
	s_cbranch_execz .LBB0_1620
	v_ashrrev_i32_e32 v1, 31, v0
	v_lshl_add_u64 v[0:1], v[0:1], 2, s[0:1]
	global_load_dword v6, v[0:1], off
.LBB0_1620:
	s_or_b64 exec, exec, s[2:3]
	v_or_b32_e32 v11, 0x80, v10
	v_add_u32_e32 v0, v11, v152
	v_cmp_lt_i32_e32 vcc, v0, v8
	s_and_saveexec_b64 s[2:3], vcc
	s_cbranch_execz .LBB0_1622
	v_ashrrev_i32_e32 v1, 31, v0
	v_lshl_add_u64 v[0:1], v[0:1], 2, s[0:1]
	global_load_dword v7, v[0:1], off
.LBB0_1622:
	s_or_b64 exec, exec, s[2:3]
	v_add_u32_e32 v0, 0x2000, v9
	v_ashrrev_i32_e32 v1, 31, v0
	v_lshrrev_b32_e32 v1, 22, v1
	v_add_u32_e32 v1, v0, v1
	v_ashrrev_i32_e32 v12, 10, v1
	v_mul_i32_i24_e32 v1, 0x400, v12
	v_sub_u32_e32 v0, v0, v1
	v_lshrrev_b32_e32 v1, 4, v0
	v_bitop3_b32 v13, v1, v0, 32 bitop3:0x6c
	v_ashrrev_i32_e32 v1, 31, v13
	v_lshrrev_b32_e32 v1, 26, v1
	v_lshlrev_b32_e32 v0, 3, v12
	v_add_u32_e32 v1, v13, v1
	v_and_b32_e32 v0, -16, v0
	v_ashrrev_i32_e32 v9, 6, v1
	v_add_u32_e32 v153, v9, v0
	v_add_u32_e32 v0, v10, v153
	v_cmp_lt_i32_e32 vcc, v0, v8
	v_mov_b32_e32 v10, 0
	v_mov_b32_e32 v14, 0
	s_and_saveexec_b64 s[2:3], vcc
	s_cbranch_execz .LBB0_1624
	v_ashrrev_i32_e32 v1, 31, v0
	v_lshl_add_u64 v[0:1], v[0:1], 2, s[0:1]
	global_load_dword v14, v[0:1], off
.LBB0_1624:
	s_or_b64 exec, exec, s[2:3]
	v_add_u32_e32 v0, v11, v153
	v_cmp_lt_i32_e32 vcc, v0, v8
	s_and_saveexec_b64 s[2:3], vcc
	s_cbranch_execz .LBB0_1626
	v_ashrrev_i32_e32 v1, 31, v0
	v_lshl_add_u64 v[0:1], v[0:1], 2, s[0:1]
	global_load_dword v10, v[0:1], off
.LBB0_1626:
	s_or_b64 exec, exec, s[2:3]
	s_waitcnt vmcnt(0)
	v_lshlrev_b32_e32 v6, 9, v6
	v_and_b32_e32 v6, 0xfffff800, v6
	v_lshlrev_b32_e32 v7, 9, v7
	v_and_b32_e32 v7, 0xfffff800, v7
	v_lshlrev_b32_e32 v14, 9, v14
	v_and_b32_e32 v14, 0xfffff800, v14
	v_lshlrev_b32_e32 v10, 9, v10
	v_and_b32_e32 v10, 0xfffff800, v10
	v_lshlrev_b32_e32 v1, 6, v9
	v_sub_u32_e32 v1, v13, v1
	v_mov_b32_e32 v8, 1
	v_lshlrev_b32_e32 v0, 5, v12
	v_ashrrev_i16_sdwa v1, v8, sext(v1) dst_sel:DWORD dst_unused:UNUSED_PAD src0_sel:DWORD src1_sel:BYTE_0
	s_add_u32 s0, s20, 0x3a87a000
	v_readlane_b32 s2, v254, 46
	v_and_b32_e32 v0, 32, v0
	v_bfe_i32 v1, v1, 0, 16
	s_addc_u32 s1, s21, 0
	v_readlane_b32 s3, v254, 47
	s_lshl_b32 s12, s2, 16
	v_add_lshl_u32 v154, v0, v1, 1
	v_lshlrev_b32_e32 v1, 6, v2
	s_lshl_b64 s[2:3], s[12:13], 11
	v_sub_u32_e32 v1, v5, v1
	s_add_u32 s2, s20, s2
	v_lshlrev_b32_e32 v0, 5, v3
	v_ashrrev_i16_sdwa v1, v8, sext(v1) dst_sel:DWORD dst_unused:UNUSED_PAD src0_sel:DWORD src1_sel:BYTE_0
	s_addc_u32 s3, s21, s3
	v_and_b32_e32 v0, 32, v0
	v_bfe_i32 v1, v1, 0, 16
	s_add_u32 s35, s2, 0x647a000
	v_readlane_b32 s2, v252, 21
	v_add_lshl_u32 v155, v0, v1, 1
	s_addc_u32 s36, s3, 0
	s_ashr_i32 s4, s2, 2
	v_lshlrev_b32_e32 v0, 1, v152
	v_lshrrev_b32_e32 v1, 2, v152
	v_and_b32_e32 v2, 3, v2
	s_mov_b32 s2, 0x1fffe0
	v_and_b32_e32 v0, 24, v0
	v_and_b32_e32 v1, 4, v1
	v_and_or_b32 v2, v152, s2, v2
	v_or3_b32 v0, v2, v1, v0
	v_and_b32_e32 v2, 3, v9
	v_and_or_b32 v2, v153, s2, v2
	s_lshl_b64 s[2:3], s[16:17], 19
	s_add_u32 s18, s35, s2
	v_lshl_add_u32 v144, v0, 11, v155
	v_lshlrev_b32_e32 v0, 1, v153
	v_lshrrev_b32_e32 v1, 2, v153
	s_addc_u32 s19, s36, s3
	s_add_i32 s37, s34, 0
	v_and_b32_e32 v0, 24, v0
	v_and_b32_e32 v1, 4, v1
	s_add_i32 m0, s37, 0x10000
	v_or3_b32 v0, v2, v1, v0
	global_load_lds_dwordx4 v144, s[18:19]
	s_add_i32 m0, s37, 0x12000
	v_lshl_add_u32 v146, v0, 11, v154
	s_add_u32 s2, s18, 0x40000
	global_load_lds_dwordx4 v146, s[18:19]
	s_addc_u32 s3, s19, 0
	s_add_i32 m0, s37, 0x14000
	v_add_u32_e32 v44, v6, v155
	global_load_lds_dwordx4 v144, s[2:3]
	s_add_i32 m0, s37, 0x16000
	s_add_i32 s38, s37, 0x2000
	global_load_lds_dwordx4 v146, s[2:3]
	s_mov_b32 m0, s37
	v_add_u32_e32 v40, v14, v154
	global_load_lds_dwordx4 v44, s[0:1]
	s_mov_b32 m0, s38
	s_add_i32 s39, s37, 0x4000
	v_add_u32_e32 v42, v7, v155
	global_load_lds_dwordx4 v40, s[0:1]
	s_mov_b32 m0, s39
	s_add_i32 s40, s37, 0x6000
	v_add_u32_e32 v46, v10, v154
	global_load_lds_dwordx4 v42, s[0:1]
	s_mov_b32 m0, s40
	v_mov_b32_e32 v145, v193
	global_load_lds_dwordx4 v46, s[0:1]
	v_mov_b32_e32 v147, v193
	s_cmp_eq_u32 s4, 1
	v_lshl_add_u64 v[0:1], s[18:19], 0, v[144:145]
	s_cselect_b64 s[2:3], -1, 0
	s_cmp_lg_u32 s4, 1
	v_lshl_add_u64 v[2:3], s[18:19], 0, v[146:147]
	s_cbranch_scc1 .LBB0_1628
	s_barrier

.LBB0_1638:
	v_cndmask_b32_e64 v0, 0, 1, s[26:27]
	v_cmp_ne_u32_e64 s[4:5], 1, v0
	s_andn2_b64 vcc, exec, s[26:27]
	v_mov_b32_e32 v161, v42
	v_mov_b32_e32 v163, v46
	v_mov_b32_e32 v162, v44
	v_mov_b32_e32 v160, v40
	s_cbranch_vccnz .LBB0_1648
	s_ashr_i32 s14, s22, 31
	s_lshr_b32 s14, s14, 29
	s_add_i32 s14, s22, s14
	s_ashr_i32 s14, s14, 3
	s_lshl_b32 s15, s14, 2
	s_add_i32 s15, s15, 0
	s_add_i32 s17, s15, 0x20100
	v_mov_b32_e32 v0, s17
	ds_read_b32 v0, v0
	s_add_i32 s15, s15, 0x201a0
	v_mov_b32_e32 v1, s15
	ds_read_b32 v4, v1
	s_mul_hi_i32 s17, s14, 0x11000
	s_waitcnt lgkmcnt(0)
	v_sub_u32_e32 v0, s48, v0
	v_lshlrev_b32_e32 v5, 8, v0
	s_mul_i32 s14, s14, 0x11000
	s_add_u32 s24, s29, s14
	v_add_u32_e32 v0, v5, v152
	s_addc_u32 s25, s33, s17
	v_cmp_lt_i32_e32 vcc, v0, v4
	v_mov_b32_e32 v3, 0
	v_mov_b32_e32 v2, 0
	s_and_saveexec_b64 s[30:31], vcc
	s_cbranch_execz .LBB0_1641
	v_ashrrev_i32_e32 v1, 31, v0
	v_lshl_add_u64 v[0:1], v[0:1], 2, s[24:25]
	global_load_dword v2, v[0:1], off
.LBB0_1641:
	s_or_b64 exec, exec, s[30:31]
	v_or_b32_e32 v6, 0x80, v5
	v_add_u32_e32 v0, v6, v152
	v_cmp_lt_i32_e32 vcc, v0, v4
	s_and_saveexec_b64 s[30:31], vcc
	s_cbranch_execz .LBB0_1643
	v_ashrrev_i32_e32 v1, 31, v0
	v_lshl_add_u64 v[0:1], v[0:1], 2, s[24:25]
	global_load_dword v3, v[0:1], off
.LBB0_1643:
	s_or_b64 exec, exec, s[30:31]
	v_add_u32_e32 v0, v5, v153
	v_cmp_lt_i32_e32 vcc, v0, v4
	v_mov_b32_e32 v5, 0
	v_mov_b32_e32 v7, 0
	s_and_saveexec_b64 s[30:31], vcc
	s_cbranch_execz .LBB0_1645
	v_ashrrev_i32_e32 v1, 31, v0
	v_lshl_add_u64 v[0:1], v[0:1], 2, s[24:25]
	global_load_dword v7, v[0:1], off
.LBB0_1645:
	s_or_b64 exec, exec, s[30:31]
	v_add_u32_e32 v0, v6, v153
	v_cmp_lt_i32_e32 vcc, v0, v4
	s_and_saveexec_b64 s[30:31], vcc
	s_cbranch_execz .LBB0_1647
	v_ashrrev_i32_e32 v1, 31, v0
	v_lshl_add_u64 v[0:1], v[0:1], 2, s[24:25]
	global_load_dword v5, v[0:1], off
.LBB0_1647:
	s_or_b64 exec, exec, s[30:31]
	s_waitcnt vmcnt(0)
	v_lshlrev_b32_e32 v2, 9, v2
	v_and_b32_e32 v2, 0xfffff800, v2
	v_lshlrev_b32_e32 v3, 9, v3
	v_and_b32_e32 v3, 0xfffff800, v3
	v_lshlrev_b32_e32 v7, 9, v7
	v_and_b32_e32 v7, 0xfffff800, v7
	v_lshlrev_b32_e32 v5, 9, v5
	v_and_b32_e32 v5, 0xfffff800, v5
	v_add_u32_e32 v160, v7, v154
	v_add_u32_e32 v161, v3, v155
	v_add_u32_e32 v162, v2, v155
	v_add_u32_e32 v163, v5, v154
